# speedup vs baseline: 1.0168x; 1.0123x over previous
.LBB1_3:
	s_mul_i32 s0, s7, s2
	s_sub_i32 s0, s6, s0
	s_add_i32 s1, s7, 1
	s_sub_i32 s6, s0, s2
	s_cmp_ge_u32 s0, s2
	s_cselect_b32 s1, s1, s7
	s_cselect_b32 s0, s6, s0
	s_add_i32 s6, s1, 1
	s_cmp_ge_u32 s0, s2
	s_cselect_b32 s0, s6, s1
	s_xor_b32 s0, s0, s5
	s_sub_i32 s0, s0, s5
	s_mul_i32 s79, s0, s76
	s_add_i32 s0, s79, s0
	s_lshl_b32 s33, s59, 7
	s_add_i32 s4, s33, s4
	s_min_i32 s80, s0, s3
	s_mul_i32 s0, s72, 0x4080
	s_mul_hi_i32 s1, s72, 0x4080
	s_add_u32 s0, s62, s0
	s_addc_u32 s1, s63, s1
	s_mul_i32 s2, s79, 0x4080
	v_and_b32_e32 v114, 63, v0
	s_mul_hi_i32 s3, s79, 0x4080
	s_add_u32 s2, s0, s2
	s_addc_u32 s3, s1, s3
	v_lshlrev_b32_e32 v108, 4, v114
	v_lshl_add_u64 v[2:3], s[2:3], 0, v[108:109]
	s_ashr_i32 s2, s4, 5
	s_mul_hi_i32 s3, s2, 0x4080
	s_mulk_i32 s2, 0x4080
	v_lshrrev_b32_e32 v27, 6, v0
	s_add_u32 s2, s62, s2
	s_addc_u32 s3, s63, s3
	v_lshlrev_b32_e32 v6, 10, v27
	v_lshl_add_u64 v[4:5], s[2:3], 0, v[108:109]
	v_mov_b32_e32 v7, v109
	v_lshl_add_u64 v[8:9], v[2:3], 0, v[6:7]
	v_lshl_add_u64 v[10:11], v[4:5], 0, v[6:7]
	v_add_u32_e32 v14, 0x3000, v6
	v_add_u32_e32 v16, 0x6000, v6
	v_add_u32_e32 v18, 0x9000, v6
	v_bfe_u32 v119, v0, 6, 2
	v_and_b32_e32 v118, 31, v0
	s_mov_b64 s[62:63], 0xc00
	v_add_u32_e32 v15, 0x15000, v6
	s_mov_b64 s[2:3], 0xc00
	v_lshl_add_u64 v[12:13], v[10:11], 0, s[2:3]
	v_readfirstlane_b32 s4, v15
	s_mov_b32 m0, s4
	s_nop 0
	global_load_lds_dwordx4 v[12:13], off
	v_add_u32_e32 v15, 0x18000, v6
	s_mov_b64 s[2:3], 0x3c00
	v_lshl_add_u64 v[12:13], v[10:11], 0, s[2:3]
	v_readfirstlane_b32 s4, v15
	s_mov_b32 m0, s4
	s_nop 0
	global_load_lds_dwordx4 v[12:13], off
	v_add_u32_e32 v15, 0x1b000, v6
	s_mov_b64 s[2:3], 0x6c00
	v_lshl_add_u64 v[12:13], v[10:11], 0, s[2:3]
	v_readfirstlane_b32 s4, v15
	s_mov_b32 m0, s4
	s_nop 0
	global_load_lds_dwordx4 v[12:13], off
	v_add_u32_e32 v15, 0x1e000, v6
	s_mov_b64 s[2:3], 0x9c00
	v_lshl_add_u64 v[12:13], v[10:11], 0, s[2:3]
	v_readfirstlane_b32 s4, v15
	s_mov_b32 m0, s4
	s_nop 0
	global_load_lds_dwordx4 v[12:13], off
	v_add_u32_e32 v15, 0x21000, v6
	s_mov_b64 s[2:3], 0xcc00
	v_lshl_add_u64 v[12:13], v[10:11], 0, s[2:3]
	v_readfirstlane_b32 s4, v15
	s_mov_b32 m0, s4
	s_nop 0
	global_load_lds_dwordx4 v[12:13], off
	v_or_b32_e32 v12, 0x90, v27
	v_min_u32_e32 v12, 0x91, v12
	v_lshlrev_b32_e32 v12, 10, v12
	v_mov_b32_e32 v13, v109
	s_nop 0
	v_readfirstlane_b32 s4, v12
	v_lshl_add_u64 v[12:13], v[4:5], 0, v[12:13]
	s_mov_b32 s2, 0xfffebc00
	s_mov_b32 s3, -1
	v_lshl_add_u64 v[12:13], v[12:13], 0, s[2:3]
	s_mov_b32 m0, s4
	s_nop 0
	global_load_lds_dwordx4 v[12:13], off
	s_movk_i32 s2, 0xdc00
	s_mov_b32 s3, -1
	v_lshl_add_u64 v[12:13], v[10:11], 0, s[2:3]
	s_mov_b64 s[2:3], 0x12000
	v_lshl_add_u64 v[142:143], v[8:9], 0, s[2:3]
	s_movk_i32 s4, 0x23f
	v_cmp_lt_u32_e32 vcc, s4, v0
	v_add_u32_e32 v15, 0x12000, v6
	s_nop 0
	v_cndmask_b32_e32 v12, v142, v12, vcc
	v_cndmask_b32_e32 v13, v143, v13, vcc
	v_readfirstlane_b32 s4, v15
	s_mov_b32 m0, s4
	s_nop 0
	global_load_lds_dwordx4 v[12:13], off
	v_mov_b32_e32 v15, v6
	v_mov_b32_e32 v12, v8
	v_mov_b32_e32 v13, v9
	v_readfirstlane_b32 s4, v15
	s_mov_b32 m0, s4
	s_nop 0
	global_load_lds_dwordx4 v[12:13], off
	v_add_u32_e32 v15, 0x3000, v6
	s_mov_b64 s[2:3], 0x3000
	v_lshl_add_u64 v[12:13], v[8:9], 0, s[2:3]
	v_readfirstlane_b32 s4, v15
	s_mov_b32 m0, s4
	s_nop 0
	global_load_lds_dwordx4 v[12:13], off
	v_add_u32_e32 v15, 0x6000, v6
	s_mov_b64 s[2:3], 0x6000
	v_lshl_add_u64 v[12:13], v[8:9], 0, s[2:3]
	v_readfirstlane_b32 s4, v15
	s_mov_b32 m0, s4
	s_nop 0
	global_load_lds_dwordx4 v[12:13], off
	v_add_u32_e32 v15, 0x9000, v6
	s_mov_b64 s[2:3], 0x9000
	v_lshl_add_u64 v[12:13], v[8:9], 0, s[2:3]
	v_readfirstlane_b32 s4, v15
	s_mov_b32 m0, s4
	s_nop 0
	global_load_lds_dwordx4 v[12:13], off
	v_add_u32_e32 v15, 0xc000, v6
	s_mov_b64 s[2:3], 0xc000
	v_lshl_add_u64 v[12:13], v[8:9], 0, s[2:3]
	v_readfirstlane_b32 s4, v15
	s_mov_b32 m0, s4
	s_nop 0
	global_load_lds_dwordx4 v[12:13], off
	v_add_u32_e32 v15, 0xf000, v6
	s_mov_b64 s[2:3], 0xf000
	v_lshl_add_u64 v[12:13], v[8:9], 0, s[2:3]
	v_readfirstlane_b32 s4, v15
	s_mov_b32 m0, s4
	s_nop 0
	global_load_lds_dwordx4 v[12:13], off
	s_mov_b32 s2, 0x14400
	s_and_b64 vcc, exec, s[68:69]
	s_cbranch_vccz .Lpx_skip
	v_lshlrev_b32_e32 v142, 2, v1
	v_mov_b32_e32 v143, v115
	v_cmp_gt_i32_e32 vcc, s78, v143
	s_nop 1
	v_cndmask_b32_e32 v143, 0, v143, vcc
	v_add_u32_e32 v143, s72, v143
	v_lshl_or_b32 v143, v143, 10, v142
	global_load_dword v120, v143, s[60:61]
	v_add_u32_e32 v143, 3, v115
	v_cmp_gt_i32_e32 vcc, s78, v143
	s_nop 1
	v_cndmask_b32_e32 v143, 0, v143, vcc
	v_add_u32_e32 v143, s72, v143
	v_lshl_or_b32 v143, v143, 10, v142
	global_load_dword v121, v143, s[60:61]
	v_add_u32_e32 v143, 6, v115
	v_cmp_gt_i32_e32 vcc, s78, v143
	s_nop 1
	v_cndmask_b32_e32 v143, 0, v143, vcc
	v_add_u32_e32 v143, s72, v143
	v_lshl_or_b32 v143, v143, 10, v142
	global_load_dword v122, v143, s[60:61]
	v_add_u32_e32 v143, 9, v115
	v_cmp_gt_i32_e32 vcc, s78, v143
	s_nop 1
	v_cndmask_b32_e32 v143, 0, v143, vcc
	v_add_u32_e32 v143, s72, v143
	v_lshl_or_b32 v143, v143, 10, v142
	global_load_dword v123, v143, s[60:61]
	v_add_u32_e32 v143, 12, v115
	v_cmp_gt_i32_e32 vcc, s78, v143
	s_nop 1
	v_cndmask_b32_e32 v143, 0, v143, vcc
	v_add_u32_e32 v143, s72, v143
	v_lshl_or_b32 v143, v143, 10, v142
	global_load_dword v124, v143, s[60:61]
	v_add_u32_e32 v143, 15, v115
	v_cmp_gt_i32_e32 vcc, s78, v143
	s_nop 1
	v_cndmask_b32_e32 v143, 0, v143, vcc
	v_add_u32_e32 v143, s72, v143
	v_lshl_or_b32 v143, v143, 10, v142
	global_load_dword v125, v143, s[60:61]
	v_add_u32_e32 v143, 18, v115
	v_cmp_gt_i32_e32 vcc, s78, v143
	s_nop 1
	v_cndmask_b32_e32 v143, 0, v143, vcc
	v_add_u32_e32 v143, s72, v143
	v_lshl_or_b32 v143, v143, 10, v142
	global_load_dword v126, v143, s[60:61]
	v_add_u32_e32 v143, 21, v115
	v_cmp_gt_i32_e32 vcc, s78, v143
	s_nop 1
	v_cndmask_b32_e32 v143, 0, v143, vcc
	v_add_u32_e32 v143, s72, v143
	v_lshl_or_b32 v143, v143, 10, v142
	global_load_dword v127, v143, s[60:61]
	v_add_u32_e32 v143, 24, v115
	v_cmp_gt_i32_e32 vcc, s78, v143
	s_nop 1
	v_cndmask_b32_e32 v143, 0, v143, vcc
	v_add_u32_e32 v143, s72, v143
	v_lshl_or_b32 v143, v143, 10, v142
	global_load_dword v128, v143, s[60:61]
	v_add_u32_e32 v143, 27, v115
	v_cmp_gt_i32_e32 vcc, s78, v143
	s_nop 1
	v_cndmask_b32_e32 v143, 0, v143, vcc
	v_add_u32_e32 v143, s72, v143
	v_lshl_or_b32 v143, v143, 10, v142
	global_load_dword v129, v143, s[60:61]
	v_add_u32_e32 v143, 30, v115
	v_cmp_gt_i32_e32 vcc, s78, v143
	s_nop 1
	v_cndmask_b32_e32 v143, 0, v143, vcc
	v_add_u32_e32 v143, s72, v143
	v_lshl_or_b32 v143, v143, 10, v142
	global_load_dword v130, v143, s[60:61]
.Lpx_skip:
	v_mul_u32_u24_e32 v4, 0x4080, v119
	s_and_b64 vcc, exec, s[68:69]
	s_cbranch_vccnz .Lw1_d
	s_waitcnt vmcnt(6)
	s_branch .Lw1_e
.Lw1_d:
	s_waitcnt vmcnt(17)
.Lw1_e:
	v_add3_u32 v5, v108, v4, s2
	v_lshl_or_b32 v4, v118, 2, v4
	s_mov_b64 s[2:3], 0x14280
	s_waitcnt lgkmcnt(0)
	s_barrier
	v_add_u32_e32 v4, 0x18400, v4
	v_lshl_add_u64 v[2:3], v[2:3], 0, s[2:3]
	ds_read_b128 v[88:91], v5
	ds_read_b128 v[84:87], v5 offset:1024
	ds_read_b128 v[80:83], v5 offset:2048
	ds_read_b128 v[76:79], v5 offset:3072
	ds_read_b128 v[72:75], v5 offset:4096
	ds_read_b128 v[68:71], v5 offset:5120
	ds_read_b128 v[64:67], v5 offset:6144
	ds_read_b128 v[60:63], v5 offset:7168
	ds_read_b128 v[56:59], v5 offset:8192
	ds_read_b128 v[52:55], v5 offset:9216
	ds_read_b128 v[48:51], v5 offset:10240
	ds_read_b128 v[44:47], v5 offset:11264
	ds_read_b128 v[40:43], v5 offset:12288
	ds_read_b128 v[36:39], v5 offset:13312
	ds_read_b128 v[32:35], v5 offset:14336
	ds_read_b128 v[28:31], v5 offset:15360
	ds_read_b32 v116, v4
	s_waitcnt lgkmcnt(0)
	v_lshl_add_u64 v[4:5], v[2:3], 0, v[6:7]
	v_add_u32_e32 v7, 0x14280, v6
	s_barrier
	v_readfirstlane_b32 s2, v7
	v_add_u32_e32 v7, 0x17280, v6
	s_mov_b32 m0, s2
	v_mov_b32_e32 v15, v109
	v_readfirstlane_b32 s2, v7
	v_add_u32_e32 v7, 0x1a280, v6
	global_load_lds_dwordx4 v[4:5], off
	v_lshl_add_u64 v[4:5], v[2:3], 0, v[14:15]
	s_mov_b32 m0, s2
	v_mov_b32_e32 v17, v109
	v_readfirstlane_b32 s2, v7
	v_add_u32_e32 v7, 0x1d280, v6
	global_load_lds_dwordx4 v[4:5], off
	v_lshl_add_u64 v[4:5], v[2:3], 0, v[16:17]
	s_mov_b32 m0, s2
	v_mov_b32_e32 v19, v109
	v_readfirstlane_b32 s2, v7
	global_load_lds_dwordx4 v[4:5], off
	v_lshl_add_u64 v[4:5], v[2:3], 0, v[18:19]
	s_mov_b32 m0, s2
	v_bfe_u32 v117, v0, 5, 1
	global_load_lds_dwordx4 v[4:5], off
	v_or_b32_e32 v4, 0xc000, v6
	v_add_u32_e32 v6, 0x20280, v6
	v_mov_b32_e32 v5, v109
	v_readfirstlane_b32 s2, v6
	v_lshl_add_u64 v[4:5], v[2:3], 0, v[4:5]
	s_mov_b32 m0, s2
	v_add_u32_e32 v131, 33, v115
	global_load_lds_dwordx4 v[4:5], off
	v_min_u32_e32 v4, 4, v27
	v_lshlrev_b32_e32 v6, 10, v4
	v_add_u32_e32 v4, 0xf000, v6
	v_mov_b32_e32 v5, v109
	v_lshl_add_u64 v[2:3], v[2:3], 0, v[4:5]
	v_add_u32_e32 v4, 0x23280, v6
	s_movk_i32 s73, 0x4080
	v_readfirstlane_b32 s2, v4
	s_mov_b32 m0, s2
	v_mov_b32_e32 v18, 0x7f800000
	global_load_lds_dwordx4 v[2:3], off
	v_mul_u32_u24_e32 v2, 0x4080, v115
	v_lshl_or_b32 v2, v117, 4, v2
	v_add_u32_e32 v132, 0x4000, v2
	v_lshl_or_b32 v2, s59, 2, v119
	v_sub_u32_e32 v134, v2, v115
	v_add_u32_e32 v2, s72, v131
	v_ashrrev_i32_e32 v3, 31, v2
	v_lshlrev_b64 v[2:3], 10, v[2:3]
	v_lshl_or_b32 v2, v1, 2, v2
	v_lshl_add_u64 v[110:111], s[0:1], 0, v[108:109]
	v_cmp_gt_i32_e64 s[0:1], s78, v131
	v_mad_u32_u24 v133, v115, s73, v108
	v_lshl_add_u64 v[112:113], s[60:61], 0, v[2:3]
	s_mov_b64 s[60:61], -1
	v_mov_b32_e32 v135, 0x4080
	v_mov_b32_e32 v136, 0xff800000
	v_mov_b32_e32 v137, 0
	s_mov_b32 s81, s79
	v_mov_b32_e32 v1, v18
	v_mov_b32_e32 v20, v18
	v_mov_b32_e32 v19, v18
	v_mov_b32_e32 v24, v18
	v_mov_b32_e32 v23, v18
	v_mov_b32_e32 v22, v18
	v_mov_b32_e32 v21, v18
	v_mov_b32_e32 v26, v18
	v_mov_b32_e32 v25, v18
	s_and_b64 vcc, exec, s[68:69]
	s_cbranch_vccnz .Lw2_d
	s_waitcnt vmcnt(7)
	s_branch .Lw2_e
.Lw2_d:
	s_waitcnt vmcnt(18)
.Lw2_e:
	s_barrier
	s_branch .LBB1_6
